# indexer unit prologue: first-pass k_idx fragment loads issued in front of the wait for the unit's q_idx/head-weight loads (one serialized round trip less per unit)
# speedup vs baseline: 1.0027x; 1.0027x over previous
; #define GAS __attribute__((address_space(1)))
; #define LAS __attribute__((address_space(3)))
; __device__ __forceinline__ void idx_unit(Frame& F, const bf16* QI, const bf16* KI, const float* WI, unsigned* MASK, int b, int j) {
;     ...
;     const size_t qrow = (size_t)b * SEQ + 32 * j + r32;
;     bf16x8 bq[4][4];
; #pragma unroll
;     for (int h = 0; h < 4; ++h)
; #pragma unroll
;         for (int kk = 0; kk < 4; ++kk) bq[h][kk] = *(const GAS bf16x8*)(QI + qrow * 256 + h * 64 + kk * 16 + hi * 8);
;     f32x4 wv = *(const GAS f32x4*)(WI + qrow * 4); wv = wv * IDX_SCALE;
;     const bf16* kbase = KI + (size_t)b * SEQ * 64 + (size_t)(hi * 32 + r32) * 8;
;     LAS unsigned* myrow = hist + r32 * IX_HS;
;     const unsigned myrow_b = (unsigned)(uintptr_t)myrow;
.LBB0_972:
	s_bfe_u32 s76, s17, 0x20006
	s_lshl_b32 s4, s76, 13
	s_lshl_b32 s5, s84, 5
	s_add_i32 s4, s4, s5
	v_or_b32_e32 v4, s4, v194
	v_mov_b32_e32 v5, v195
	s_lshl_b32 s8, s4, 9
	v_sub_u32_e32 v8, v226, v228
	v_lshl_add_u32 v6, v8, 4, s8
	v_mov_b32_e32 v7, 0
	s_mov_b64 s[40:41], 0x1000
	v_lshl_add_u64 v[6:7], v[208:209], 0, v[6:7]
	v_lshl_add_u64 v[8:9], v[6:7], 0, s[40:41]
	v_lshl_add_u64 v[10:11], v[8:9], 0, s[40:41]
	v_lshl_add_u64 v[12:13], v[10:11], 0, s[40:41]
	global_load_dwordx4 v[82:85], v[6:7], off
	global_load_dwordx4 v[86:89], v[6:7], off offset:1024
	global_load_dwordx4 v[90:93], v[6:7], off offset:2048
	global_load_dwordx4 v[94:97], v[6:7], off offset:3072
	global_load_dwordx4 v[98:101], v[8:9], off
	global_load_dwordx4 v[102:105], v[8:9], off offset:1024
	global_load_dwordx4 v[106:109], v[8:9], off offset:2048
	global_load_dwordx4 v[110:113], v[8:9], off offset:3072
	global_load_dwordx4 v[114:117], v[10:11], off
	global_load_dwordx4 v[118:121], v[10:11], off offset:1024
	global_load_dwordx4 v[122:125], v[10:11], off offset:2048
	global_load_dwordx4 v[126:129], v[10:11], off offset:3072
	global_load_dwordx4 v[130:133], v[12:13], off
	global_load_dwordx4 v[134:137], v[12:13], off offset:1024
	global_load_dwordx4 v[138:141], v[12:13], off offset:2048
	global_load_dwordx4 v[142:145], v[12:13], off offset:3072
	v_lshl_add_u64 v[4:5], v[4:5], 4, s[88:89]
	global_load_dwordx4 v[4:7], v[4:5], off
	s_lshl_b32 s92, s76, 20
	v_lshl_add_u64 v[12:13], v[210:211], 0, s[92:93]
	s_min_i32 s6, s23, s84
	s_min_i32 s4, s21, s84
	s_ashr_i32 s7, s6, 31
	s_ashr_i32 s5, s4, 31
	s_lshl_b64 s[6:7], s[6:7], 12
	s_lshl_b64 s[4:5], s[4:5], 12
	v_lshl_add_u64 v[8:9], v[12:13], 0, s[6:7]
	v_lshl_add_u64 v[10:11], v[12:13], 0, s[4:5]
	v_lshl_add_u64 v[12:13], v[12:13], 0, s[90:91]
	global_load_dwordx4 v[158:161], v[8:9], off offset:3072
	global_load_dwordx4 v[166:169], v[8:9], off offset:2048
	global_load_dwordx4 v[170:173], v[8:9], off offset:1024
	global_load_dwordx4 v[174:177], v[8:9], off
	global_load_dwordx4 v[146:149], v[10:11], off offset:3072
	global_load_dwordx4 v[150:153], v[10:11], off offset:2048
	global_load_dwordx4 v[154:157], v[10:11], off offset:1024
	global_load_dwordx4 v[162:165], v[10:11], off
	global_load_dwordx4 v[64:67], v[12:13], off offset:3072
	global_load_dwordx4 v[68:71], v[12:13], off offset:2048
	global_load_dwordx4 v[72:75], v[12:13], off offset:1024
	global_load_dwordx4 v[76:79], v[12:13], off
	s_cmp_gt_u32 s84, 7
	s_mov_b32 s4, 0x3d800000
	s_cselect_b64 s[94:95], -1, 0
	s_and_b64 vcc, exec, s[94:95]
	s_waitcnt vmcnt(0)
	v_pk_mul_f32 v[214:215], v[6:7], s[4:5] op_sel_hi:[1,0]
	v_pk_mul_f32 v[216:217], v[4:5], s[4:5] op_sel_hi:[1,0]
	s_mov_b64 s[4:5], -1
	s_cbranch_vccnz .LBB0_974
	s_mov_b64 s[4:5], 0
	v_mov_b32_e32 v2, v215
; #define IX_MF(ACC, H, KK) ACC = __builtin_amdgcn_mfma_f32_32x32x16_bf16(a[KK], bq[H][KK], ACC, 0, 0, 0)
; #define IX_RS0(ACC, W, R) do { _Pragma("unroll") for (int r = (R); r < (R) + 4; ++r) { const float x = ACC[r]; sc[r] = __builtin_fmaf(W, IX_RELU(x), 0.0f); } } while (0)
; #define IX_RS(ACC, W, R) do { _Pragma("unroll") for (int r = (R); r < (R) + 4; ++r) { const float x = ACC[r]; sc[r] = __builtin_fmaf(W, IX_RELU(x), sc[r]); } } while (0)
; #define IX_PIN(ACC, VACC, R) asm volatile("" : "+v"(ACC), "+v"(VACC), "+v"(sc[R]), "+v"(sc[(R) + 1]), "+v"(sc[(R) + 2]), "+v"(sc[(R) + 3]))
; template <bool PREV> __device__ __forceinline__ void idx_half1(float (&sc)[16], f32x16& acc0, f32x16& acc1, f32x16& acc2, f32x16& acc3, const bf16x8 (&a)[4], const bf16x8 (&bq)[4][4], const f32x4 wv) {
;     acc0 = (f32x16){};
; #pragma unroll
;     for (int kk = 0; kk < 4; ++kk) { IX_MF(acc0, 0, kk); if constexpr (PREV) { IX_RS(acc2, wv[2], 4 * kk); IX_PIN(acc0, acc2, 4 * kk); } }
;     acc1 = (f32x16){};
; #pragma unroll
;     for (int kk = 0; kk < 4; ++kk) { IX_MF(acc1, 1, kk); if constexpr (PREV) { IX_RS(acc3, wv[3], 4 * kk); IX_PIN(acc1, acc3, 4 * kk); } }
; }
; __device__ __forceinline__ void idx_half2(float (&sc)[16], f32x16& acc0, f32x16& acc1, f32x16& acc2, f32x16& acc3, const bf16x8 (&a)[4], const bf16x8 (&bq)[4][4], const f32x4 wv) {
;     acc2 = (f32x16){};
; #pragma unroll
;     for (int kk = 0; kk < 4; ++kk) { IX_MF(acc2, 2, kk); IX_RS0(acc0, wv[0], 4 * kk); IX_PIN(acc2, acc0, 4 * kk); }
;     acc3 = (f32x16){};
; #pragma unroll
;     for (int kk = 0; kk < 4; ++kk) { IX_MF(acc3, 3, kk); IX_RS(acc1, wv[1], 4 * kk); IX_PIN(acc3, acc1, 4 * kk); }
; }
.LBB0_974:
	s_lshl_b32 s92, s76, 20
	s_andn2_b64 vcc, exec, s[4:5]
	v_lshl_add_u64 v[218:219], v[210:211], 0, s[92:93]
	s_cbranch_vccnz .LBB0_990
	s_cmp_gt_i32 s38, s84
	v_mov_b32_e32 v212, v226
	v_mov_b32_e32 v230, v228
	v_mov_b32_e32 v231, v194
	s_cbranch_scc1 .LBB0_995
	s_min_i32 s6, s23, s84
	s_min_i32 s4, s21, s84
	s_ashr_i32 s7, s6, 31
	s_ashr_i32 s5, s4, 31
	s_lshl_b64 s[6:7], s[6:7], 12
	s_lshl_b64 s[4:5], s[4:5], 12
	v_lshl_add_u64 v[8:9], v[218:219], 0, s[6:7]
	v_lshl_add_u64 v[4:5], v[218:219], 0, s[90:91]
	v_lshl_add_u64 v[6:7], v[218:219], 0, s[4:5]
	v_lshlrev_b32_e32 v213, 2, v230
	s_cmp_gt_i32 s21, s84
	v_cmp_lt_i32_e64 s[40:41], v213, v231
	v_or_b32_e32 v232, 2, v213
	v_or_b32_e32 v233, 3, v213
	v_add_u32_e32 v235, 8, v213
	v_add_u32_e32 v234, 9, v213
	v_add_u32_e32 v236, 10, v213
	v_add_u32_e32 v237, 11, v213
	v_add_u32_e32 v239, 16, v213
	v_add_u32_e32 v238, 17, v213
	v_add_u32_e32 v240, 18, v213
	v_add_u32_e32 v242, 19, v213
	v_add_u32_e32 v243, 24, v213
	v_add_u32_e32 v241, 25, v213
	v_add_u32_e32 v248, 26, v213
	v_add_u32_e32 v249, 27, v213
	s_waitcnt vmcnt(0)
	v_mfma_f32_32x32x16_bf16 v[32:47], v[76:79], v[82:85], 0
	v_mfma_f32_32x32x16_bf16 v[32:47], v[72:75], v[86:89], v[32:47]
	v_mfma_f32_32x32x16_bf16 v[32:47], v[68:71], v[90:93], v[32:47]
	v_mfma_f32_32x32x16_bf16 v[48:63], v[76:79], v[98:101], 0
	v_mfma_f32_32x32x16_bf16 v[32:47], v[64:67], v[94:97], v[32:47]
	v_mfma_f32_32x32x16_bf16 v[48:63], v[72:75], v[102:105], v[48:63]
	s_nop 10
	v_max_i32_e32 v1, 0, v32
	v_max_i32_e32 v2, 0, v34
	v_fma_f32 v224, v216, v1, 0
	v_max_i32_e32 v1, 0, v33
	v_fma_f32 v222, v216, v2, 0
	v_max_i32_e32 v2, 0, v35
	v_fma_f32 v1, v216, v1, 0
	v_mfma_f32_32x32x16_bf16 v[48:63], v[68:71], v[106:109], v[48:63]
	v_fma_f32 v5, v216, v2, 0
	v_mfma_f32_32x32x16_bf16 v[16:31], v[76:79], v[114:117], 0
	s_nop 0
	v_max_i32_e32 v2, 0, v36
	v_fma_f32 v220, v216, v2, 0
	v_max_i32_e32 v2, 0, v37
	v_fma_f32 v221, v216, v2, 0
	v_max_i32_e32 v2, 0, v38
	v_fma_f32 v6, v216, v2, 0
	v_max_i32_e32 v2, 0, v39
	v_mfma_f32_32x32x16_bf16 v[16:31], v[72:75], v[118:121], v[16:31]
	v_fma_f32 v7, v216, v2, 0
	s_nop 0
	v_max_i32_e32 v2, 0, v40
	v_fma_f32 v8, v216, v2, 0
	v_max_i32_e32 v2, 0, v41
	v_fma_f32 v9, v216, v2, 0
	v_mfma_f32_32x32x16_bf16 v[48:63], v[64:67], v[110:113], v[48:63]
	v_max_i32_e32 v2, 0, v42
	v_fma_f32 v10, v216, v2, 0
	v_max_i32_e32 v2, 0, v43
	v_fma_f32 v11, v216, v2, 0
	v_mfma_f32_32x32x16_bf16 v[16:31], v[68:71], v[122:125], v[16:31]
	s_nop 0
	v_max_i32_e32 v2, 0, v44
	v_fma_f32 v12, v216, v2, 0
	v_max_i32_e32 v2, 0, v45
	v_fma_f32 v13, v216, v2, 0
	v_max_i32_e32 v2, 0, v46
	v_fma_f32 v14, v216, v2, 0
	v_max_i32_e32 v2, 0, v47
	v_fma_f32 v15, v216, v2, 0
	v_max_i32_e32 v2, 0, v48
	v_fmac_f32_e32 v224, v217, v2
	v_max_i32_e32 v2, 0, v49
	v_mfma_f32_32x32x16_bf16 v[16:31], v[64:67], v[126:129], v[16:31]
	v_fmac_f32_e32 v1, v217, v2
	v_max_i32_e32 v2, 0, v50
	v_fmac_f32_e32 v222, v217, v2
	v_max_i32_e32 v2, 0, v51
	v_fmac_f32_e32 v5, v217, v2
	v_mfma_f32_32x32x16_bf16 v[32:47], v[76:79], v[130:133], 0
	s_nop 0
	v_max_i32_e32 v2, 0, v52
	v_fmac_f32_e32 v220, v217, v2
	v_max_i32_e32 v2, 0, v53
	v_fmac_f32_e32 v221, v217, v2
	v_max_i32_e32 v2, 0, v54
	v_fmac_f32_e32 v6, v217, v2
	v_max_i32_e32 v2, 0, v55
	v_mfma_f32_32x32x16_bf16 v[32:47], v[72:75], v[134:137], v[32:47]
	v_fmac_f32_e32 v7, v217, v2
	s_nop 0
	v_max_i32_e32 v2, 0, v56
	v_fmac_f32_e32 v8, v217, v2
	v_max_i32_e32 v2, 0, v57
	v_fmac_f32_e32 v9, v217, v2
	v_max_i32_e32 v2, 0, v58
	v_fmac_f32_e32 v10, v217, v2
	v_max_i32_e32 v2, 0, v59
	v_mfma_f32_32x32x16_bf16 v[32:47], v[68:71], v[138:141], v[32:47]
	v_fmac_f32_e32 v11, v217, v2
	s_nop 0
	v_max_i32_e32 v2, 0, v60
	v_fmac_f32_e32 v12, v217, v2
	v_max_i32_e32 v2, 0, v61
	v_fmac_f32_e32 v13, v217, v2
	v_max_i32_e32 v2, 0, v62
	v_fmac_f32_e32 v14, v217, v2
	v_max_i32_e32 v2, 0, v63
	v_mfma_f32_32x32x16_bf16 v[32:47], v[64:67], v[142:145], v[32:47]
	v_fmac_f32_e32 v15, v217, v2
	s_cbranch_scc1 .LBB0_991
	v_readlane_b32 s4, v252, 35
	s_min_i32 s72, s4, s84
	v_cmp_gt_i32_e64 s[42:43], v213, v231
	v_cmp_gt_i32_e64 s[44:45], v232, v231
	v_cmp_gt_i32_e64 s[46:47], v233, v231
	v_cmp_gt_i32_e64 s[48:49], v235, v231
	v_cmp_gt_i32_e64 s[50:51], v234, v231
	v_cmp_gt_i32_e64 s[52:53], v236, v231
	v_cmp_gt_i32_e64 s[54:55], v237, v231
	v_cmp_gt_i32_e64 s[56:57], v239, v231
	v_cmp_gt_i32_e64 s[58:59], v238, v231
	v_cmp_gt_i32_e64 s[60:61], v240, v231
	v_cmp_gt_i32_e64 s[62:63], v242, v231
	v_cmp_gt_i32_e64 s[64:65], v243, v231
	v_cmp_gt_i32_e64 s[66:67], v241, v231
	v_cmp_gt_i32_e64 s[68:69], v248, v231
	v_cmp_gt_i32_e64 s[70:71], v249, v231
	s_sub_i32 s4, 0, s84
	v_readlane_b32 s5, v252, 36
	s_branch .LBB0_979
